# speedup vs baseline: 1.0142x; 1.0033x over previous
.LBB2_5:
	s_lshl_b32 s66, s16, 3
	s_ashr_i32 s67, s16, 31
	s_add_i32 s5, s66, s67
	s_xor_b32 s68, s5, s67
	v_cvt_f32_u32_e32 v1, s68
	s_add_i32 s4, s17, s4
	s_sub_i32 s17, 0, s68
	s_abs_i32 s16, s4
	v_rcp_iflag_f32_e32 v1, v1
	s_ashr_i32 s5, s4, 31
	s_xor_b32 s5, s5, s67
	v_lshlrev_b32_e32 v2, 4, v0
	v_mul_f32_e32 v1, 0x4f7ffffe, v1
	v_cvt_u32_f32_e32 v1, v1
	v_lshrrev_b32_e32 v3, 3, v0
	v_bfe_u32 v4, v0, 2, 4
	v_and_or_b32 v3, v3, 48, v4
	v_readfirstlane_b32 s18, v1
	s_mul_i32 s17, s17, s18
	s_mul_hi_u32 s17, s18, s17
	s_add_i32 s69, s18, s17
	s_mul_hi_u32 s17, s16, s69
	s_mul_i32 s18, s17, s68
	s_sub_i32 s16, s16, s18
	s_add_i32 s19, s17, 1
	s_sub_i32 s18, s16, s68
	s_cmp_ge_u32 s16, s68
	s_cselect_b32 s17, s19, s17
	s_cselect_b32 s16, s18, s16
	s_add_i32 s18, s17, 1
	s_cmp_ge_u32 s16, s68
	s_cselect_b32 s16, s18, s17
	s_xor_b32 s16, s16, s5
	s_sub_i32 s5, s16, s5
	s_lshl_b32 s18, s5, 3
	s_sub_i32 s16, s3, s18
	s_min_i32 s16, s16, 8
	s_abs_i32 s17, s16
	v_cvt_f32_u32_e32 v1, s17
	s_sub_i32 s20, 0, s17
	s_mul_i32 s5, s5, s66
	s_sub_i32 s4, s4, s5
	v_rcp_iflag_f32_e32 v1, v1
	s_abs_i32 s5, s4
	s_xor_b32 s19, s4, s16
	s_ashr_i32 s19, s19, 31
	v_mul_f32_e32 v1, 0x4f7ffffe, v1
	v_cvt_u32_f32_e32 v1, v1
	v_mov_b32_e32 v163, 0
	v_lshlrev_b32_e32 v4, 6, v0
	v_lshlrev_b32_e32 v6, 2, v0
	v_readfirstlane_b32 s21, v1
	s_mul_i32 s20, s20, s21
	s_mul_hi_u32 s20, s21, s20
	s_add_i32 s21, s21, s20
	s_mul_hi_u32 s20, s5, s21
	s_mul_i32 s21, s20, s17
	s_sub_i32 s5, s5, s21
	s_add_i32 s22, s20, 1
	s_sub_i32 s21, s5, s17
	s_cmp_ge_u32 s5, s17
	s_cselect_b32 s20, s22, s20
	s_cselect_b32 s5, s21, s5
	s_add_i32 s21, s20, 1
	s_cmp_ge_u32 s5, s17
	s_cselect_b32 s5, s21, s20
	s_xor_b32 s5, s5, s19
	s_sub_i32 s5, s5, s19
	s_lshl_b32 s50, s5, 8
	s_mul_i32 s16, s5, s16
	s_ashr_i32 s51, s50, 31
	s_sub_i32 s19, s4, s16
	v_and_b32_e32 v1, 32, v0
	s_lshl_b64 s[4:5], s[50:51], 10
	v_bitop3_b32 v1, v2, v1, 48 bitop3:0x6c
	v_readfirstlane_b32 s16, v0
	s_add_u32 s4, s10, s4
	v_and_or_b32 v1, v0, 64, v1
	s_addc_u32 s5, s11, s5
	s_lshl_b32 s16, s16, 4
	v_lshl_or_b32 v1, v3, 10, v1
	s_and_b32 s20, s16, 0x7ffffc00
	s_add_i32 s21, 0, 0x10000
	s_add_i32 s19, s19, s18
	s_add_i32 s22, s21, s20
	v_mov_b32_e32 v2, v1
	s_lshl_b32 s44, s19, 8
	s_mov_b32 m0, s22
	v_mov_b32_e32 v162, v1
	s_ashr_i32 s45, s44, 31
	global_load_lds_dwordx4 v2, s[4:5]
	s_mov_b64 s[16:17], 0x10000
	v_lshl_add_u64 v[2:3], s[4:5], 0, v[162:163]
	s_add_i32 m0, s22, 0x2000
	s_lshl_b64 s[4:5], s[44:45], 10
	v_lshl_add_u64 v[2:3], v[2:3], 0, s[16:17]
	s_add_u32 s4, s8, s4
	global_load_lds_dwordx4 v[2:3], off
	s_addc_u32 s5, s9, s5
	s_add_i32 s70, s20, 0
	v_mov_b32_e32 v2, v1
	s_mov_b32 m0, s70
	v_mov_b32_e32 v162, v1
	global_load_lds_dwordx4 v2, s[4:5]
	s_add_i32 s71, s70, 0x2000
	v_lshl_add_u64 v[2:3], s[4:5], 0, v[162:163]
	s_or_b32 s4, s50, 0x80
	s_ashr_i32 s5, s4, 31
	s_lshl_b64 s[4:5], s[4:5], 10
	s_add_u32 s4, s10, s4
	v_lshl_add_u64 v[2:3], v[2:3], 0, s[16:17]
	s_mov_b32 m0, s71
	s_addc_u32 s5, s11, s5
	s_add_i32 s22, 0, 0x14000
	global_load_lds_dwordx4 v[2:3], off
	s_add_i32 s18, s22, s20
	v_mov_b32_e32 v2, v1
	s_mov_b32 m0, s18
	v_mov_b32_e32 v162, v1
	global_load_lds_dwordx4 v2, s[4:5]
	s_add_i32 m0, s18, 0x2000
	v_lshl_add_u64 v[2:3], s[4:5], 0, v[162:163]
	s_or_b32 s4, s44, 0x80
	s_ashr_i32 s5, s4, 31
	s_lshl_b64 s[4:5], s[4:5], 10
	v_lshl_add_u64 v[2:3], v[2:3], 0, s[16:17]
	s_add_u32 s4, s8, s4
	global_load_lds_dwordx4 v[2:3], off
	s_addc_u32 s5, s9, s5
	s_add_i32 s72, s70, 0x4000
	v_mov_b32_e32 v2, v1
	s_mov_b32 m0, s72
	v_mov_b32_e32 v162, v1
	global_load_lds_dwordx4 v2, s[4:5]
	s_add_i32 s73, s70, 0x6000
	v_lshl_add_u64 v[2:3], s[4:5], 0, v[162:163]
	v_lshl_add_u64 v[2:3], v[2:3], 0, s[16:17]
	s_mov_b32 m0, s73
	s_load_dwordx2 s[18:19], s[0:1], 0x10
	global_load_lds_dwordx4 v[2:3], off
	v_and_b32_e32 v3, 48, v0
	v_and_b32_e32 v5, 0x3c0, v4
	v_and_b32_e32 v6, 32, v6
	v_lshrrev_b32_e32 v2, 8, v0
	v_bitop3_b32 v3, v3, v6, v5 bitop3:0x36
	s_add_i32 s4, 0, 0x18000
	v_cmp_eq_u32_e64 s[0:1], 1, v2
	v_add_u32_e32 v7, s4, v3
	s_add_i32 s4, 0, 0x1c000
	v_lshlrev_b32_e32 v2, 13, v2
	v_add_u32_e32 v5, s21, v3
	v_add_u32_e32 v6, s22, v3
	v_add_u32_e32 v8, s4, v3
	s_movk_i32 s4, 0x100
	v_and_b32_e32 v4, 0x3000, v4
	v_add_u32_e32 v3, 0, v3
	v_or_b32_e32 v9, 0x800, v2
	v_or_b32_e32 v10, 0x1000, v2
	v_or_b32_e32 v11, 0x1800, v2
	s_movk_i32 s74, 0x3c0
	v_cmp_gt_u32_e64 s[4:5], s4, v0
	s_mov_b64 s[56:57], -1
	s_mov_b32 s87, 0
	s_mov_b64 s[20:21], 0x80
	s_mov_b64 s[22:23], 0x10080
	v_add_u32_e32 v164, v5, v4
	v_add_u32_e32 v165, v3, v2
	v_add_u32_e32 v166, v3, v9
	v_add_u32_e32 v167, v3, v10
	v_add_u32_e32 v168, v3, v11
	s_mov_b64 s[24:25], 0x20080
	s_mov_b64 s[26:27], 0x30080
	v_add_u32_e32 v169, v6, v4
	s_mov_b64 s[28:29], 0x100
	s_mov_b64 s[30:31], 0x10100
	s_mov_b64 s[34:35], 0x20100
	s_mov_b64 s[36:37], 0x30100
	v_add_u32_e32 v170, v7, v4
	v_add_u32_e32 v171, v8, v4
	s_mov_b64 s[38:39], 0x180
	s_mov_b64 s[40:41], 0x10180
	s_mov_b64 s[42:43], 0x20180
	s_mov_b64 s[46:47], 0x30180
	s_mov_b64 s[48:49], 0x380
	s_branch .LBB2_8

.LBB2_10:
	s_or_b64 exec, exec, s[52:53]
	s_xor_b64 s[54:55], s[56:57], -1
	s_mov_b64 s[52:53], -1
	s_and_b64 vcc, exec, s[54:55]
	s_cbranch_vccz .LBB2_12
	s_waitcnt vmcnt(32)
	s_mov_b32 s87, 1
	s_mov_b64 s[52:53], 0

.LBB2_14:
	s_ashr_i32 s51, s50, 31
	s_lshl_b64 s[52:53], s[50:51], 10
	s_add_u32 s52, s10, s52
	s_addc_u32 s53, s11, s53
	v_mov_b32_e32 v162, v1
	s_barrier
	s_add_i32 s78, s70, 0x18000
	v_lshl_add_u64 v[2:3], s[52:53], 0, v[162:163]
	s_ashr_i32 s45, s44, 31
	v_lshl_add_u64 v[2:3], v[2:3], 0, s[20:21]
	s_mov_b32 m0, s78
	v_mov_b32_e32 v162, v1
	s_add_i32 s79, s70, 0x1a000
	s_lshl_b64 s[54:55], s[44:45], 10
	global_load_lds_dwordx4 v[2:3], off
	s_add_u32 s54, s8, s54
	v_lshl_add_u64 v[2:3], s[52:53], 0, v[162:163]
	v_lshl_add_u64 v[2:3], v[2:3], 0, s[22:23]
	s_mov_b32 m0, s79
	s_addc_u32 s55, s9, s55
	v_mov_b32_e32 v162, v1
	s_or_b32 s56, s50, 0x80
	global_load_lds_dwordx4 v[2:3], off
	s_add_i32 s45, s70, 0x8000
	v_lshl_add_u64 v[2:3], s[54:55], 0, v[162:163]
	s_ashr_i32 s57, s56, 31
	v_lshl_add_u64 v[2:3], v[2:3], 0, s[20:21]
	s_mov_b32 m0, s45
	v_mov_b32_e32 v162, v1
	s_add_i32 s80, s70, 0xa000
	s_lshl_b64 s[56:57], s[56:57], 10
	global_load_lds_dwordx4 v[2:3], off
	s_add_u32 s56, s10, s56
	v_lshl_add_u64 v[2:3], s[54:55], 0, v[162:163]
	v_lshl_add_u64 v[2:3], v[2:3], 0, s[22:23]
	s_mov_b32 m0, s80
	s_addc_u32 s57, s11, s57
	v_mov_b32_e32 v162, v1
	global_load_lds_dwordx4 v[2:3], off
	s_add_i32 s82, s70, 0x1c000
	v_lshl_add_u64 v[2:3], s[56:57], 0, v[162:163]
	v_lshl_add_u64 v[2:3], v[2:3], 0, s[20:21]
	s_mov_b32 m0, s82
	v_mov_b32_e32 v162, v1
	global_load_lds_dwordx4 v[2:3], off
	s_add_i32 s84, s70, 0x1e000
	v_lshl_add_u64 v[2:3], s[56:57], 0, v[162:163]
	v_lshl_add_u64 v[2:3], v[2:3], 0, s[22:23]
	s_mov_b32 m0, s84
	v_mov_b32_e32 v50, 0
	global_load_lds_dwordx4 v[2:3], off
	s_waitcnt lgkmcnt(0)
	s_lshr_b32 s86, s44, 10
	s_cmp_eq_u32 s86, 1
	s_cselect_b32 s88, s14, s6
	s_cselect_b32 s89, s15, s7
	s_cmp_eq_u32 s86, 0
	s_cselect_b32 s88, s12, s88
	s_cselect_b32 s89, s13, s89
	s_and_b32 s86, s44, 0x3ff
	s_lshl_b32 s86, s86, 2
	s_add_u32 s88, s88, s86
	s_addc_u32 s89, s89, 0
	v_and_b32_e32 v184, 63, v0
	v_lshlrev_b32_e32 v184, 4, v184
	s_mov_b32 m0, 0x20000
	s_nop 0
	global_load_lds_dwordx4 v184, s[88:89]
	s_cmp_eq_u32 s87, 0
	s_cbranch_scc1 .Lg2_w6
	s_waitcnt vmcnt(39)
	s_branch .Lg2_wd
.Lg2_w6:
	s_waitcnt vmcnt(7)
.Lg2_wd:
	s_mov_b32 s85, -2
	s_mov_b64 s[56:57], 0
	v_mov_b32_e32 v51, v50
	v_mov_b32_e32 v52, v50
	v_mov_b32_e32 v53, v50
	v_mov_b32_e32 v66, v50
	v_mov_b32_e32 v67, v50
	v_mov_b32_e32 v68, v50
	v_mov_b32_e32 v69, v50
	v_mov_b32_e32 v82, v50
	v_mov_b32_e32 v83, v50
	v_mov_b32_e32 v84, v50
	v_mov_b32_e32 v85, v50
	v_mov_b32_e32 v86, v50
	v_mov_b32_e32 v87, v50
	v_mov_b32_e32 v88, v50
	v_mov_b32_e32 v89, v50
	v_mov_b32_e32 v98, v50
	v_mov_b32_e32 v99, v50
	v_mov_b32_e32 v100, v50
	v_mov_b32_e32 v101, v50
	v_mov_b32_e32 v110, v50
	v_mov_b32_e32 v111, v50
	v_mov_b32_e32 v112, v50
	v_mov_b32_e32 v113, v50
	v_mov_b32_e32 v122, v50
	v_mov_b32_e32 v123, v50
	v_mov_b32_e32 v124, v50
	v_mov_b32_e32 v125, v50
	v_mov_b32_e32 v126, v50
	v_mov_b32_e32 v127, v50
	v_mov_b32_e32 v128, v50
	v_mov_b32_e32 v129, v50
	v_mov_b32_e32 v118, v50
	v_mov_b32_e32 v119, v50
	v_mov_b32_e32 v120, v50
	v_mov_b32_e32 v121, v50
	v_mov_b32_e32 v114, v50
	v_mov_b32_e32 v115, v50
	v_mov_b32_e32 v116, v50
	v_mov_b32_e32 v117, v50
	v_mov_b32_e32 v106, v50
	v_mov_b32_e32 v107, v50
	v_mov_b32_e32 v108, v50
	v_mov_b32_e32 v109, v50
	v_mov_b32_e32 v102, v50
	v_mov_b32_e32 v103, v50
	v_mov_b32_e32 v104, v50
	v_mov_b32_e32 v105, v50
	v_mov_b32_e32 v94, v50
	v_mov_b32_e32 v95, v50
	v_mov_b32_e32 v96, v50
	v_mov_b32_e32 v97, v50
	v_mov_b32_e32 v90, v50
	v_mov_b32_e32 v91, v50
	v_mov_b32_e32 v92, v50
	v_mov_b32_e32 v93, v50
	v_mov_b32_e32 v78, v50
	v_mov_b32_e32 v79, v50
	v_mov_b32_e32 v80, v50
	v_mov_b32_e32 v81, v50
	v_mov_b32_e32 v74, v50
	v_mov_b32_e32 v75, v50
	v_mov_b32_e32 v76, v50
	v_mov_b32_e32 v77, v50
	v_mov_b32_e32 v62, v50
	v_mov_b32_e32 v63, v50
	v_mov_b32_e32 v64, v50
	v_mov_b32_e32 v65, v50
	v_mov_b32_e32 v54, v50
	v_mov_b32_e32 v55, v50
	v_mov_b32_e32 v56, v50
	v_mov_b32_e32 v57, v50
	v_mov_b32_e32 v42, v50
	v_mov_b32_e32 v43, v50
	v_mov_b32_e32 v44, v50
	v_mov_b32_e32 v45, v50
	v_mov_b32_e32 v34, v50
	v_mov_b32_e32 v35, v50
	v_mov_b32_e32 v36, v50
	v_mov_b32_e32 v37, v50
	v_mov_b32_e32 v26, v50
	v_mov_b32_e32 v27, v50
	v_mov_b32_e32 v28, v50
	v_mov_b32_e32 v29, v50
	v_mov_b32_e32 v18, v50
	v_mov_b32_e32 v19, v50
	v_mov_b32_e32 v20, v50
	v_mov_b32_e32 v21, v50
	v_mov_b32_e32 v10, v50
	v_mov_b32_e32 v11, v50
	v_mov_b32_e32 v12, v50
	v_mov_b32_e32 v13, v50
	v_mov_b32_e32 v2, v50
	v_mov_b32_e32 v3, v50
	v_mov_b32_e32 v4, v50
	v_mov_b32_e32 v5, v50
	v_mov_b32_e32 v70, v50
	v_mov_b32_e32 v71, v50
	v_mov_b32_e32 v72, v50
	v_mov_b32_e32 v73, v50
	v_mov_b32_e32 v58, v50
	v_mov_b32_e32 v59, v50
	v_mov_b32_e32 v60, v50
	v_mov_b32_e32 v61, v50
	v_mov_b32_e32 v46, v50
	v_mov_b32_e32 v47, v50
	v_mov_b32_e32 v48, v50
	v_mov_b32_e32 v49, v50
	v_mov_b32_e32 v38, v50
	v_mov_b32_e32 v39, v50
	v_mov_b32_e32 v40, v50
	v_mov_b32_e32 v41, v50
	v_mov_b32_e32 v30, v50
	v_mov_b32_e32 v31, v50
	v_mov_b32_e32 v32, v50
	v_mov_b32_e32 v33, v50
	v_mov_b32_e32 v22, v50
	v_mov_b32_e32 v23, v50
	v_mov_b32_e32 v24, v50
	v_mov_b32_e32 v25, v50
	v_mov_b32_e32 v14, v50
	v_mov_b32_e32 v15, v50
	v_mov_b32_e32 v16, v50
	v_mov_b32_e32 v17, v50
	v_mov_b32_e32 v6, v50
	v_mov_b32_e32 v7, v50
	v_mov_b32_e32 v8, v50
	v_mov_b32_e32 v9, v50
	s_barrier

.LBB2_26:
	s_endpgm
	s_nop 0
	s_nop 0
	s_nop 0
	s_nop 0
	s_nop 0
	s_nop 0
	s_nop 0
	s_nop 0
	s_nop 0
	s_nop 0
	s_nop 0
	s_nop 0
	s_nop 0
	s_nop 0
	s_nop 0
	s_nop 0
	s_nop 0
	s_nop 0
	s_nop 0
	s_nop 0
	s_nop 0
	s_nop 0
	s_nop 0
	s_nop 0
	s_nop 0
	s_nop 0
	s_nop 0
	s_nop 0
	s_nop 0
	s_nop 0
	s_nop 0
	s_nop 0
	s_nop 0
	s_nop 0
	s_nop 0
	s_nop 0
	s_nop 0
	s_nop 0
	s_nop 0
	s_nop 0
	s_nop 0
	s_nop 0
	s_nop 0
	s_nop 0
	s_nop 0
	s_nop 0
	s_nop 0
	s_nop 0
	s_nop 0
	s_nop 0
	s_nop 0
	s_endpgm
